# baseline (speedup 1.0000x reference)
_Z11attn_kernelPKDF16_S0_PDF16_P15HIP_vector_typeIfLj2EE:
	s_getpc_b64 s[38:39]
	v_lshlrev_b32_e32 v240, 7, v0
	v_min_u32_e32 v240, 0x3380, v240
	global_load_dword v241, v240, s[38:39]
	s_mov_b32 s5, 0
	s_mov_b32 s28, s3
	s_load_dwordx8 s[20:27], s[0:1], 0x0
	s_mov_b32 s3, s5
	s_lshl_b64 s[0:1], s[4:5], 12
	s_lshl_b64 s[2:3], s[2:3], 8
	s_add_u32 s0, s0, s2
	v_lshrrev_b32_e32 v1, 6, v0
	s_addc_u32 s1, s1, s3
	v_and_b32_e32 v160, 31, v0
	s_lshl_b64 s[2:3], s[0:1], 8
	v_lshlrev_b32_e32 v162, 5, v1
	s_waitcnt lgkmcnt(0)
	s_add_u32 s2, s20, s2
	v_or_b32_e32 v2, v162, v160
	v_bfe_u32 v54, v0, 5, 1
	s_addc_u32 s3, s21, s3
	v_lshlrev_b32_e32 v164, 8, v2
	v_mov_b32_e32 v165, 0
	v_lshl_add_u64 v[2:3], s[2:3], 0, v[164:165]
	v_lshlrev_b32_e32 v164, 4, v54
	v_lshl_add_u64 v[2:3], v[2:3], 0, v[164:165]
	global_load_dwordx4 v[156:159], v[2:3], off
	global_load_dwordx4 v[152:155], v[2:3], off offset:32
	global_load_dwordx4 v[148:151], v[2:3], off offset:64
	global_load_dwordx4 v[144:147], v[2:3], off offset:96
	global_load_dwordx4 v[140:143], v[2:3], off offset:128
	global_load_dwordx4 v[136:139], v[2:3], off offset:160
	global_load_dwordx4 v[132:135], v[2:3], off offset:192
	global_load_dwordx4 v[128:131], v[2:3], off offset:224
	s_ashr_i32 s29, s28, 31
	v_bfe_u32 v55, v0, 2, 3
	s_lshl_b64 s[2:3], s[4:5], 20
	s_lshl_b64 s[20:21], s[28:29], 18
	v_lshl_or_b32 v2, v1, 3, v55
	s_add_u32 s4, s22, s2
	v_lshrrev_b32_e32 v3, 2, v2
	s_addc_u32 s7, s23, s3
	v_xor_b32_e32 v4, v3, v0
	s_add_u32 s6, s4, s20
	v_and_b32_e32 v5, 32, v0
	v_lshlrev_b32_e32 v4, 3, v4
	v_lshlrev_b32_e32 v1, 11, v1
	s_addc_u32 s7, s7, s21
	v_lshlrev_b32_e32 v164, 8, v2
	v_and_or_b32 v4, v4, 24, v5
	v_add_u32_e32 v173, 0, v1
	v_lshl_add_u64 v[2:3], s[6:7], 0, v[164:165]
	v_lshlrev_b32_e32 v164, 1, v4
	v_readfirstlane_b32 s4, v173
	v_add_u32_e32 v6, 0x400, v173
	v_lshl_add_u64 v[2:3], v[2:3], 0, v[164:165]
	s_mov_b64 s[6:7], 0x80
	s_mov_b32 m0, s4
	v_readfirstlane_b32 s4, v6
	v_add_u32_e32 v6, 0x4000, v173
	v_lshl_add_u64 v[4:5], v[2:3], 0, s[6:7]
	global_load_lds_dwordx4 v[2:3], off
	s_mov_b32 m0, s4
	s_mov_b64 s[6:7], 0x4000
	v_readfirstlane_b32 s4, v6
	global_load_lds_dwordx4 v[4:5], off
	v_lshl_add_u64 v[4:5], v[2:3], 0, s[6:7]
	s_mov_b32 m0, s4
	s_mov_b64 s[6:7], 0x4080
	global_load_lds_dwordx4 v[4:5], off
	v_add_u32_e32 v4, 0x4400, v173
	v_lshl_add_u64 v[2:3], v[2:3], 0, s[6:7]
	v_readfirstlane_b32 s4, v4
	s_mov_b32 m0, s4
	s_movk_i32 s4, 0x1c0
	global_load_lds_dwordx4 v[2:3], off
	v_lshlrev_b32_e32 v2, 8, v0
	v_and_b32_e32 v2, 0x1800, v2
	v_lshlrev_b32_e32 v3, 6, v0
	v_and_or_b32 v6, v3, s4, v2
	v_xor_b32_e32 v2, v54, v55
	v_lshlrev_b32_e32 v2, 4, v2
	v_and_or_b32 v175, v2, 48, v6
	s_waitcnt vmcnt(2)
	v_add_u32_e32 v172, 0, v175
	s_waitcnt lgkmcnt(0)
	s_barrier
	ds_read_b128 v[2:5], v172
	ds_read_b128 v[34:37], v172 offset:512
	v_bitop3_b32 v7, v54, v55, 2 bitop3:0x36
	v_lshlrev_b32_e32 v7, 4, v7
	v_and_or_b32 v176, v7, 48, v6
	v_add_u32_e32 v174, 0, v176
	ds_read_b128 v[18:21], v174
	ds_read_b128 v[38:41], v174 offset:512
	s_mov_b32 s33, 0x41200000
	s_cmp_lg_u32 0, -1
	s_cselect_b32 s37, 0, 0
	s_waitcnt vmcnt(2) lgkmcnt(0)
	v_mfma_f32_32x32x16_f16 v[2:17], v[2:5], v[156:159], 0
	s_movk_i32 s4, 0x110
	v_and_b32_e32 v161, 63, v0
	v_lshl_or_b32 v1, v55, 8, v1
	s_mov_b32 s18, s5
	s_mov_b32 s19, s5
	s_mov_b32 s6, s5
	s_mov_b32 s7, s5
	v_mfma_f32_32x32x16_f16 v[2:17], v[18:21], v[152:155], v[2:17]
	ds_read_b128 v[18:21], v172 offset:8192
	ds_read_b128 v[42:45], v172 offset:8704
	ds_read_b128 v[46:49], v174 offset:8192
	ds_read_b128 v[50:53], v174 offset:8704
	s_mov_b32 s8, s5
	s_mov_b32 s9, s5
	s_mov_b32 s10, s5
	s_mov_b32 s11, s5
	s_mov_b32 s12, s5
	s_waitcnt lgkmcnt(3)
	v_mfma_f32_32x32x16_f16 v[18:33], v[18:21], v[156:159], 0
	s_mov_b32 s13, s5
	s_mov_b32 s14, s5
	s_mov_b32 s15, s5
	s_mov_b32 s16, s5
	s_mov_b32 s17, s5
	s_mov_b32 s36, 1
	s_mov_b32 s34, -1
	s_waitcnt lgkmcnt(1)
	v_mfma_f32_32x32x16_f16 v[18:33], v[46:49], v[152:155], v[18:33]
	s_mov_b32 s35, 2
	s_mov_b64 s[30:31], 0x8000
	v_mfma_f32_32x32x16_f16 v[2:17], v[34:37], v[148:151], v[2:17]
	v_mfma_f32_32x32x16_f16 v[18:33], v[42:45], v[148:151], v[18:33]
	v_mfma_f32_32x32x16_f16 v[2:17], v[38:41], v[144:147], v[2:17]
	ds_read_b128 v[34:37], v172 offset:1024
	ds_read_b128 v[38:41], v172 offset:1536
	s_waitcnt lgkmcnt(2)
	v_mfma_f32_32x32x16_f16 v[18:33], v[50:53], v[144:147], v[18:33]
	s_waitcnt lgkmcnt(1)
	v_mfma_f32_32x32x16_f16 v[2:17], v[34:37], v[140:143], v[2:17]
	ds_read_b128 v[34:37], v172 offset:9216
	ds_read_b128 v[42:45], v172 offset:9728
	s_waitcnt lgkmcnt(1)
	v_mfma_f32_32x32x16_f16 v[18:33], v[34:37], v[140:143], v[18:33]
	ds_read_b128 v[34:37], v174 offset:1024
	ds_read_b128 v[46:49], v174 offset:1536
	s_waitcnt lgkmcnt(1)
	v_mfma_f32_32x32x16_f16 v[2:17], v[34:37], v[136:139], v[2:17]
	ds_read_b128 v[34:37], v174 offset:9216
	ds_read_b128 v[50:53], v174 offset:9728
	v_mfma_f32_32x32x16_f16 v[2:17], v[38:41], v[132:135], v[2:17]
	s_waitcnt lgkmcnt(1)
	v_mfma_f32_32x32x16_f16 v[18:33], v[34:37], v[136:139], v[18:33]
	v_mov_b32_e32 v34, 0xf149f2ca
	v_mfma_f32_32x32x16_f16 v[2:17], v[46:49], v[128:131], v[2:17]
	v_mfma_f32_32x32x16_f16 v[18:33], v[42:45], v[132:135], v[18:33]
	s_nop 10
	v_max_f32_e32 v35, v3, v3
	v_max_f32_e32 v36, v2, v2
	v_max_f32_e32 v35, v36, v35
	v_max3_f32 v35, v35, v4, v5
	v_max3_f32 v35, v35, v6, v7
	v_max3_f32 v35, v35, v8, v9
	v_max3_f32 v35, v35, v10, v11
	s_waitcnt lgkmcnt(0)
	v_mfma_f32_32x32x16_f16 v[18:33], v[50:53], v[128:131], v[18:33]
	v_max3_f32 v35, v35, v12, v13
	v_max3_f32 v35, v35, v14, v15
	v_max3_f32 v35, v35, v16, v17
	s_nop 8
	v_max3_f32 v35, v35, v18, v19
	v_max3_f32 v35, v35, v20, v21
	v_max3_f32 v35, v35, v22, v23
	v_max3_f32 v35, v35, v24, v25
	v_max3_f32 v35, v35, v26, v27
	v_max3_f32 v35, v35, v28, v29
	v_max3_f32 v35, v35, v30, v31
	v_max3_f32 v35, v35, v32, v33
	v_mov_b32_e32 v36, v35
	s_nop 1
	v_permlane32_swap_b32_e32 v35, v36
	v_max_f32_e32 v36, v36, v36
	v_max_f32_e32 v35, v35, v35
	v_max_f32_e32 v35, v35, v36
	v_add_f32_e32 v36, 0x7149f2ca, v35
	v_cmp_ge_f32_e32 vcc, s33, v36
	s_cmp_eq_u64 vcc, exec
	v_max_f32_e32 v35, 0xf149f2ca, v35
	s_cselect_b64 vcc, -1, 0
	v_cndmask_b32_e32 v168, v35, v34, vcc
	v_sub_f32_e32 v96, v18, v168
	v_sub_f32_e32 v97, v19, v168
	v_lshlrev_b32_e32 v18, 4, v0
	v_lshrrev_b32_e32 v19, 4, v0
	v_sub_f32_e32 v98, v20, v168
	v_and_b32_e32 v18, 0xc0, v18
	v_bitop3_b32 v19, v19, v54, 1 bitop3:0x6c
	v_lshlrev_b32_e32 v20, 3, v0
	v_sub_f32_e32 v99, v21, v168
	v_lshl_or_b32 v18, v54, 11, v18
	v_lshlrev_b32_e32 v19, 5, v19
	v_and_b32_e32 v21, 8, v20
	v_or3_b32 v18, v18, v21, v19
	v_and_b32_e32 v19, 16, v20
	v_sub_f32_e32 v0, 0xf149f2ca, v35
	v_add3_u32 v163, v19, s37, v18
	v_bitop3_b32 v169, v18, s4, v19 bitop3:0x36
	v_exp_f32_e32 v18, v0
	s_add_u32 s2, s2, s20
	v_sub_f32_e32 v2, v2, v168
	v_sub_f32_e32 v3, v3, v168
	v_sub_f32_e32 v4, v4, v168
	v_sub_f32_e32 v5, v5, v168
	v_sub_f32_e32 v6, v6, v168
	v_sub_f32_e32 v7, v7, v168
	v_sub_f32_e32 v8, v8, v168
	v_sub_f32_e32 v9, v9, v168
	v_sub_f32_e32 v10, v10, v168
	v_sub_f32_e32 v11, v11, v168
	v_sub_f32_e32 v12, v12, v168
	v_sub_f32_e32 v13, v13, v168
	v_sub_f32_e32 v14, v14, v168
	v_sub_f32_e32 v15, v15, v168
	v_sub_f32_e32 v16, v16, v168
	v_sub_f32_e32 v17, v17, v168
	s_addc_u32 s3, s3, s21
	s_mov_b32 s4, s5
	v_exp_f32_e32 v127, v2
	v_exp_f32_e32 v180, v3
	v_exp_f32_e32 v125, v4
	v_exp_f32_e32 v179, v5
	v_exp_f32_e32 v123, v6
	v_exp_f32_e32 v126, v7
	v_exp_f32_e32 v122, v8
	v_exp_f32_e32 v124, v9
	v_exp_f32_e32 v119, v10
	v_exp_f32_e32 v121, v11
	v_exp_f32_e32 v117, v12
	v_exp_f32_e32 v120, v13
	v_exp_f32_e32 v115, v14
	v_exp_f32_e32 v118, v15
	v_exp_f32_e32 v114, v16
	v_exp_f32_e32 v116, v17
	v_or3_b32 v0, s2, v1, v164
	v_mov_b32_e32 v1, s3
	v_lshlrev_b32_e32 v164, 3, v54
	v_mov_b64_e32 v[62:63], s[18:19]
	v_lshl_add_u64 v[0:1], s[22:23], 0, v[0:1]
	s_mov_b64 s[2:3], 0xc080
	v_mov_b64_e32 v[48:49], s[4:5]
	v_sub_f32_e32 v100, v22, v168
	v_sub_f32_e32 v101, v23, v168
	v_sub_f32_e32 v102, v24, v168
	v_sub_f32_e32 v103, v25, v168
	v_sub_f32_e32 v104, v26, v168
	v_sub_f32_e32 v105, v27, v168
	v_sub_f32_e32 v106, v28, v168
	v_sub_f32_e32 v107, v29, v168
	v_sub_f32_e32 v108, v30, v168
	v_sub_f32_e32 v109, v31, v168
	v_sub_f32_e32 v110, v32, v168
	v_sub_f32_e32 v111, v33, v168
	v_lshl_add_u64 v[170:171], v[0:1], 0, s[2:3]
	s_movk_i32 s2, 0xbf80
	s_movk_i32 s20, 0xc000
	s_movk_i32 s22, 0xff80
	v_mov_b32_e32 v166, 1.0
	v_mov_b64_e32 v[60:61], s[16:17]
	v_mov_b64_e32 v[58:59], s[14:15]
	v_mov_b64_e32 v[56:57], s[12:13]
	v_mov_b64_e32 v[54:55], s[10:11]
	v_mov_b64_e32 v[52:53], s[8:9]
	v_mov_b64_e32 v[50:51], s[6:7]
	v_mov_b64_e32 v[32:33], v[48:49]
	v_mov_b64_e32 v[16:17], v[48:49]
	v_mov_b64_e32 v[0:1], v[48:49]
	s_mov_b32 s3, -1
	s_mov_b32 s21, -1
	s_mov_b32 s23, -1
	v_add_u32_e32 v167, s37, v169
	v_mov_b64_e32 v[34:35], v[50:51]
	v_mov_b64_e32 v[36:37], v[52:53]
	v_mov_b64_e32 v[38:39], v[54:55]
	v_mov_b64_e32 v[40:41], v[56:57]
	v_mov_b64_e32 v[42:43], v[58:59]
	v_mov_b64_e32 v[44:45], v[60:61]
	v_mov_b64_e32 v[46:47], v[62:63]
	v_mov_b64_e32 v[18:19], v[50:51]
	v_mov_b64_e32 v[20:21], v[52:53]
	v_mov_b64_e32 v[22:23], v[54:55]
	v_mov_b64_e32 v[24:25], v[56:57]
	v_mov_b64_e32 v[26:27], v[58:59]
	v_mov_b64_e32 v[28:29], v[60:61]
	v_mov_b64_e32 v[30:31], v[62:63]
	v_mov_b64_e32 v[2:3], v[50:51]
	v_mov_b64_e32 v[4:5], v[52:53]
	v_mov_b64_e32 v[6:7], v[54:55]
	v_mov_b64_e32 v[8:9], v[56:57]
	v_mov_b64_e32 v[10:11], v[58:59]
	v_mov_b64_e32 v[12:13], v[60:61]
	v_mov_b64_e32 v[14:15], v[62:63]

.LBB1_11:
	v_add_f32_e32 v82, v112, v113
	v_add_f32_e32 v101, v80, v81
	v_fmac_f32_e32 v82, v165, v166
	ds_read_b64_tr_b16 v[84:85], v163 offset:0
	ds_read_b64_tr_b16 v[86:87], v167 offset:0
	ds_read_b64_tr_b16 v[88:89], v163 offset:0x1000
	ds_read_b64_tr_b16 v[90:91], v167 offset:0x1000
	ds_read_b64_tr_b16 v[92:93], v163 offset:0x2000
	ds_read_b64_tr_b16 v[94:95], v167 offset:0x2000
	ds_read_b64_tr_b16 v[96:97], v163 offset:0x3000
	ds_read_b64_tr_b16 v[98:99], v167 offset:0x3000
	ds_read_b64_tr_b16 v[104:105], v163 offset:0x200
	ds_read_b64_tr_b16 v[106:107], v167 offset:0x200
	ds_read_b64_tr_b16 v[108:109], v163 offset:0x1200
	ds_read_b64_tr_b16 v[110:111], v167 offset:0x1200
	ds_read_b64_tr_b16 v[112:113], v163 offset:0x2200
	ds_read_b64_tr_b16 v[114:115], v167 offset:0x2200
	ds_read_b64_tr_b16 v[116:117], v163 offset:0x3200
	ds_read_b64_tr_b16 v[118:119], v167 offset:0x3200
	s_nop 0
	s_waitcnt lgkmcnt(14)
	v_mfma_f32_32x32x16_f16 v[48:63], v[84:87], v[76:79], v[48:63]
	ds_read_b64_tr_b16 v[84:85], v163 offset:0x400
	ds_read_b64_tr_b16 v[86:87], v167 offset:0x400
	s_waitcnt lgkmcnt(8)
	v_mfma_f32_32x32x16_f16 v[32:47], v[104:107], v[76:79], v[32:47]
	v_mfma_f32_32x32x16_f16 v[48:63], v[88:91], v[72:75], v[48:63]
	ds_read_b64_tr_b16 v[88:89], v163 offset:0x1400
	ds_read_b64_tr_b16 v[90:91], v167 offset:0x1400
	s_waitcnt lgkmcnt(8)
	v_mfma_f32_32x32x16_f16 v[32:47], v[108:111], v[72:75], v[32:47]
	v_mfma_f32_32x32x16_f16 v[48:63], v[92:95], v[68:71], v[48:63]
	ds_read_b64_tr_b16 v[92:93], v163 offset:0x2400
	ds_read_b64_tr_b16 v[94:95], v167 offset:0x2400
	ds_read_b64_tr_b16 v[104:105], v163 offset:0x3400
	ds_read_b64_tr_b16 v[106:107], v167 offset:0x3400
	ds_read_b64_tr_b16 v[108:109], v163 offset:0x600
	ds_read_b64_tr_b16 v[110:111], v167 offset:0x600
	s_waitcnt lgkmcnt(12)
	v_mfma_f32_32x32x16_f16 v[32:47], v[112:115], v[68:71], v[32:47]
	v_mfma_f32_32x32x16_f16 v[48:63], v[96:99], v[64:67], v[48:63]
	ds_read_b64_tr_b16 v[96:97], v163 offset:0x1600
	ds_read_b64_tr_b16 v[98:99], v167 offset:0x1600
	ds_read_b64_tr_b16 v[112:113], v163 offset:0x2600
	ds_read_b64_tr_b16 v[114:115], v167 offset:0x2600
	ds_read_b64_tr_b16 v[120:121], v163 offset:0x3600
	ds_read_b64_tr_b16 v[122:123], v167 offset:0x3600
	s_waitcnt lgkmcnt(15)
	v_mfma_f32_32x32x16_f16 v[32:47], v[116:119], v[64:67], v[32:47]
	s_waitcnt lgkmcnt(14)
	v_mfma_f32_32x32x16_f16 v[16:31], v[84:87], v[76:79], v[16:31]
	s_lshl_b64 s[2:3], s[28:29], 14
	v_mov_b32_e32 v163, 0
	s_add_u32 s0, s0, s2
	v_cmp_lt_u32_e32 vcc, 31, v161
	s_addc_u32 s1, s1, s3
	s_waitcnt lgkmcnt(6)
	v_mfma_f32_32x32x16_f16 v[0:15], v[108:111], v[76:79], v[0:15]
	v_mfma_f32_32x32x16_f16 v[16:31], v[88:91], v[72:75], v[16:31]
	s_waitcnt lgkmcnt(4)
	v_mfma_f32_32x32x16_f16 v[0:15], v[96:99], v[72:75], v[0:15]
	v_mfma_f32_32x32x16_f16 v[16:31], v[92:95], v[68:71], v[16:31]
	s_waitcnt lgkmcnt(2)
	v_mfma_f32_32x32x16_f16 v[0:15], v[112:115], v[68:71], v[0:15]
	v_mov_b32_e32 v69, v163
	v_mfma_f32_32x32x16_f16 v[16:31], v[104:107], v[64:67], v[16:31]
	s_waitcnt lgkmcnt(0)
	v_mfma_f32_32x32x16_f16 v[0:15], v[120:123], v[64:67], v[0:15]
	s_and_saveexec_b64 s[2:3], vcc
	s_xor_b64 s[2:3], exec, s[2:3]
	s_or_saveexec_b64 s[2:3], s[2:3]
	v_fmac_f32_e32 v101, v82, v102
	v_lshl_add_u64 v[64:65], s[0:1], 0, v[162:163]
	s_xor_b64 exec, exec, s[2:3]
	s_cbranch_execz .LBB1_13
	v_lshl_add_u64 v[66:67], v[64:65], 3, s[26:27]
	v_lshlrev_b32_e32 v70, 3, v160
	v_mov_b32_e32 v71, 0
	v_lshl_add_u64 v[66:67], v[66:67], 0, v[70:71]
	global_store_dwordx2 v[66:67], v[100:101], off sc1
